# scan state: per-k decay vector read once per block (ds_read_b32) and applied with v_mul_f32_dpp row_newbcast instead of 4 broadcast ds_read_b128 + v_pk_mul; plus hoisted prep staging loads
# speedup vs baseline: 1.0026x; 1.0026x over previous
.LBB0_1113:
	s_and_b64 s[0:1], s[6:7], exec
	s_mov_b32 s0, 0x3d800000
	s_cselect_b32 s0, s0, 0x3fc00000
	v_readlane_b32 s3, v255, 13
	v_lshl_or_b32 v2, s8, 7, v123
	s_lshl_b32 s1, s3, 11
	v_or_b32_e32 v188, s0, v2
	s_movk_i32 s0, 0xf800
	s_add_i32 s2, s1, 0x1000
	v_readlane_b32 s1, v255, 11
	v_writelane_b32 v255, s0, 25
	s_lshl_b32 s3, s3, 8
	v_mov_b32_e32 v2, 0
	v_writelane_b32 v255, s2, 31
	v_or_b32_e32 v189, s1, v101
	s_mov_b32 s4, 0
	v_mov_b32_e32 v190, v167
	s_mov_b32 s0, 0
	v_mov_b32_e32 v3, v2
	v_mov_b32_e32 v4, v2
	v_mov_b32_e32 v5, v2
	v_mov_b32_e32 v6, v2
	v_mov_b32_e32 v7, v2
	v_mov_b32_e32 v8, v2
	v_mov_b32_e32 v9, v2
	v_mov_b32_e32 v10, v2
	v_mov_b32_e32 v11, v2
	v_mov_b32_e32 v12, v2
	v_mov_b32_e32 v13, v2
	v_mov_b32_e32 v14, v2
	v_mov_b32_e32 v15, v2
	v_mov_b32_e32 v16, v2
	v_mov_b32_e32 v17, v2
	v_writelane_b32 v255, s3, 23
	v_readlane_b32 s14, v254, 35
	v_readlane_b32 s15, v254, 36
	s_nop 1
	s_andn2_b64 vcc, exec, s[14:15]
	s_cbranch_vccnz .Lscan_pre_skip
	v_add_u32_e32 v246, v115, v155
	v_bfe_u32 v248, v0, 4, 2
	v_mul_u32_u24_e32 v248, 0x240, v248
	v_bfe_u32 v249, v0, 2, 2
	v_mul_u32_u24_e32 v249, 0x90, v249
	v_and_b32_e32 v250, 3, v0
	v_add_u32_e32 v248, v248, v249
	v_lshl_add_u32 v248, v250, 3, v248
	v_bfe_u32 v249, v0, 6, 2
	v_and_b32_e32 v251, 12, v0
	v_lshl_add_u32 v251, v251, 4, v113
	v_lshl_add_u32 v251, v250, 2, v251
	v_lshl_add_u32 v250, v249, 5, v248
	v_add_u32_e32 v247, 0x1200, v246
	ds_read2_b64 v[18:21], v246 offset1:4
	ds_read2_b64 v[22:25], v246 offset0:8 offset1:12
	ds_read_b64_tr_b16 v[66:67], v250 offset:18432

.LBB0_1114:
	v_writelane_b32 v255, s0, 11
	s_and_b32 s5, s0, 1
	v_readlane_b32 s0, v254, 35
	v_readlane_b32 s1, v254, 36
	s_andn2_b64 vcc, exec, s[0:1]
	s_mov_b64 s[76:77], -1
	v_cndmask_b32_e64 v194, 0, 1, s[0:1]
	v_cmp_ne_u32_e64 s[8:9], 1, v194
	s_mul_i32 s0, s5, 0x1e00
	v_writelane_b32 v255, s8, 17
	v_writelane_b32 v255, s9, 18
	v_writelane_b32 v255, s5, 13
	s_cbranch_vccnz .LBB0_1116
	v_readlane_b32 s0, v255, 13
	s_nop 1
	s_nop 0
	s_mul_i32 s1, s0, 0x1e00
	s_lshl_b32 s0, s0, 13
	v_add_u32_e32 v252, s1, v166
	v_add_u32_e32 v253, s0, v165
	ds_read2_b64 v[68:71], v252 offset1:80
	v_cvt_pk_bf16_f32 v198, v2, v3
	v_cvt_pk_bf16_f32 v199, v4, v5
	v_cvt_pk_bf16_f32 v202, v10, v11
	v_cvt_pk_bf16_f32 v203, v12, v13
	v_cvt_pk_bf16_f32 v200, v6, v7
	v_cvt_pk_bf16_f32 v201, v8, v9
	v_cvt_pk_bf16_f32 v204, v14, v15
	v_cvt_pk_bf16_f32 v205, v16, v17
	ds_read2_b64 v[26:29], v247 offset1:4
	ds_read2_b64 v[30:33], v247 offset0:8 offset1:12
	ds_read2_b64 v[72:75], v252 offset0:160 offset1:240
	v_mfma_f32_16x16x16_bf16 v[206:209], v[18:19], v[198:199], 0
	v_mfma_f32_16x16x16_bf16 v[210:213], v[22:23], v[202:203], 0
	ds_read_b64_tr_b16 v[34:35], v248 offset:9216
	ds_read_b64_tr_b16 v[36:37], v248 offset:9248
	ds_read_b64_tr_b16 v[38:39], v248 offset:9280
	ds_read_b64_tr_b16 v[40:41], v248 offset:9312
	v_mfma_f32_16x16x16_bf16 v[206:209], v[20:21], v[200:201], v[206:209]
	v_mfma_f32_16x16x16_bf16 v[210:213], v[24:25], v[204:205], v[210:213]
	ds_read_b64_tr_b16 v[42:43], v248 offset:13824
	ds_read_b64_tr_b16 v[44:45], v248 offset:13856
	ds_read_b64_tr_b16 v[46:47], v248 offset:13888
	ds_read_b64_tr_b16 v[48:49], v248 offset:13920
	s_waitcnt lgkmcnt(11)
	v_mfma_f32_16x16x16_bf16 v[210:213], v[68:69], v[66:67], v[210:213]
	s_waitcnt lgkmcnt(10)
	v_mfma_f32_16x16x16_bf16 v[214:217], v[26:27], v[198:199], 0
	s_waitcnt lgkmcnt(9)
	v_mfma_f32_16x16x16_bf16 v[218:221], v[30:31], v[202:203], 0
	v_mfma_f32_16x16x16_bf16 v[214:217], v[28:29], v[200:201], v[214:217]
	v_mfma_f32_16x16x16_bf16 v[218:221], v[32:33], v[204:205], v[218:221]
	ds_read_b32 v50, v251 offset:33792
	ds_read_b32 v51, v251 offset:34048
	v_add_u32_e32 v246, 0x900, v246
	ds_read2_b64 v[76:79], v246 offset1:4
	ds_read2_b64 v[80:83], v246 offset0:8 offset1:12
	v_pk_add_f32 v[206:207], v[206:207], v[210:211]
	v_pk_add_f32 v[208:209], v[208:209], v[212:213]
	v_cvt_pk_bf16_f32 v242, v206, v207
	v_cvt_pk_bf16_f32 v243, v208, v209
	ds_read_b64_tr_b16 v[84:85], v250 offset:20736
	v_add_u32_e32 v252, 0xf00, v252
	s_waitcnt lgkmcnt(13)
	ds_read2_b64 v[86:89], v252 offset1:80
	v_mfma_f32_16x16x16_bf16 v[238:241], v[74:75], v[242:243], 0
	v_mfma_f32_16x16x16_bf16 v[214:217], v[70:71], v[66:67], v[214:217]
	s_waitcnt lgkmcnt(12)
	v_mfma_f32_16x16x16_bf16 v[2:5], v[34:35], v[66:67], v[2:5]
	v_mfma_f32_16x16x16_bf16 v[6:9], v[36:37], v[66:67], v[6:9]
	s_waitcnt lgkmcnt(10)
	v_mfma_f32_16x16x16_bf16 v[10:13], v[38:39], v[66:67], v[10:13]
	v_mfma_f32_16x16x16_bf16 v[14:17], v[40:41], v[66:67], v[14:17]
	ds_read2_b64 v[90:93], v252 offset0:160 offset1:240
	v_add_u32_e32 v247, 0x900, v247
	ds_read2_b64 v[26:29], v247 offset1:4
	ds_read2_b64 v[30:33], v247 offset0:8 offset1:12
	v_cvt_pk_bf16_f32 v244, -v238, -v239
	v_cvt_pk_bf16_f32 v245, -v240, -v241
	ds_read_b64_tr_b16 v[34:35], v248 offset:11520
	s_waitcnt lgkmcnt(13)
	ds_read_b64_tr_b16 v[36:37], v248 offset:11552
	s_waitcnt lgkmcnt(13)
	ds_read_b64_tr_b16 v[38:39], v248 offset:11584
	s_waitcnt lgkmcnt(13)
	ds_read_b64_tr_b16 v[40:41], v248 offset:11616
	v_mfma_f32_16x16x16_bf16 v[2:5], v[42:43], v[244:245], v[2:5]
	v_mfma_f32_16x16x16_bf16 v[6:9], v[44:45], v[244:245], v[6:9]
	s_waitcnt lgkmcnt(13)
	v_mfma_f32_16x16x16_bf16 v[10:13], v[46:47], v[244:245], v[10:13]
	v_mfma_f32_16x16x16_bf16 v[14:17], v[48:49], v[244:245], v[14:17]
	v_mfma_f32_16x16x16_bf16 v[218:221], v[72:73], v[244:245], v[218:221]
	ds_read_b64_tr_b16 v[42:43], v248 offset:16128
	s_waitcnt lgkmcnt(13)
	ds_read_b64_tr_b16 v[44:45], v248 offset:16160
	s_waitcnt lgkmcnt(13)
	ds_read_b64_tr_b16 v[46:47], v248 offset:16192
	s_waitcnt lgkmcnt(13)
	ds_read_b64_tr_b16 v[48:49], v248 offset:16224
	v_mul_f32_dpp v2, v50, v2 row_newbcast:0 row_mask:0xf bank_mask:0xf
	v_mul_f32_dpp v3, v50, v3 row_newbcast:1 row_mask:0xf bank_mask:0xf
	v_mul_f32_dpp v4, v50, v4 row_newbcast:2 row_mask:0xf bank_mask:0xf
	v_mul_f32_dpp v5, v50, v5 row_newbcast:3 row_mask:0xf bank_mask:0xf
	v_mul_f32_dpp v6, v50, v6 row_newbcast:4 row_mask:0xf bank_mask:0xf
	v_mul_f32_dpp v7, v50, v7 row_newbcast:5 row_mask:0xf bank_mask:0xf
	v_mul_f32_dpp v8, v50, v8 row_newbcast:6 row_mask:0xf bank_mask:0xf
	v_mul_f32_dpp v9, v50, v9 row_newbcast:7 row_mask:0xf bank_mask:0xf
	v_mul_f32_dpp v10, v50, v10 row_newbcast:8 row_mask:0xf bank_mask:0xf
	v_mul_f32_dpp v11, v50, v11 row_newbcast:9 row_mask:0xf bank_mask:0xf
	v_mul_f32_dpp v12, v50, v12 row_newbcast:10 row_mask:0xf bank_mask:0xf
	v_mul_f32_dpp v13, v50, v13 row_newbcast:11 row_mask:0xf bank_mask:0xf
	v_mul_f32_dpp v14, v50, v14 row_newbcast:12 row_mask:0xf bank_mask:0xf
	v_mul_f32_dpp v15, v50, v15 row_newbcast:13 row_mask:0xf bank_mask:0xf
	v_mul_f32_dpp v16, v50, v16 row_newbcast:14 row_mask:0xf bank_mask:0xf
	v_mul_f32_dpp v17, v50, v17 row_newbcast:15 row_mask:0xf bank_mask:0xf
	v_pk_add_f32 v[214:215], v[214:215], v[218:219]
	v_pk_add_f32 v[216:217], v[216:217], v[220:221]
	s_waitcnt lgkmcnt(13)
	ds_write2st64_b32 v253, v214, v215 offset0:0 offset1:1
	s_waitcnt lgkmcnt(13)
	ds_write2st64_b32 v253, v216, v217 offset0:2 offset1:3
	v_cvt_pk_bf16_f32 v198, v2, v3
	v_cvt_pk_bf16_f32 v199, v4, v5
	v_cvt_pk_bf16_f32 v202, v10, v11
	v_cvt_pk_bf16_f32 v203, v12, v13
	v_cvt_pk_bf16_f32 v200, v6, v7
	v_cvt_pk_bf16_f32 v201, v8, v9
	v_cvt_pk_bf16_f32 v204, v14, v15
	v_cvt_pk_bf16_f32 v205, v16, v17
	v_add_u32_e32 v246, v115, v155
	v_bfe_u32 v248, v0, 4, 2
	v_mul_u32_u24_e32 v248, 0x240, v248
	v_bfe_u32 v249, v0, 2, 2
	v_mul_u32_u24_e32 v249, 0x90, v249
	v_and_b32_e32 v250, 3, v0
	v_add_u32_e32 v248, v248, v249
	v_lshl_add_u32 v248, v250, 3, v248
	v_bfe_u32 v249, v0, 6, 2
	v_add_u32_e32 v246, 0x8600, v246
	v_add_u32_e32 v248, 0x8600, v248
	v_and_b32_e32 v251, 12, v0
	v_lshl_add_u32 v251, v251, 4, v113
	v_lshl_add_u32 v251, v250, 2, v251
	v_add_u32_e32 v251, 0x8600, v251
	v_lshl_add_u32 v250, v249, 5, v248
	v_add_u32_e32 v247, 0x1200, v246
	s_waitcnt lgkmcnt(13)
	ds_read2_b64 v[18:21], v246 offset1:4
	s_waitcnt lgkmcnt(13)
	ds_read2_b64 v[22:25], v246 offset0:8 offset1:12
	s_waitcnt lgkmcnt(13)
	ds_read_b64_tr_b16 v[66:67], v250 offset:18432
	v_mfma_f32_16x16x16_bf16 v[206:209], v[76:77], v[198:199], 0
	v_mfma_f32_16x16x16_bf16 v[210:213], v[80:81], v[202:203], 0
	v_mfma_f32_16x16x16_bf16 v[206:209], v[78:79], v[200:201], v[206:209]
	v_mfma_f32_16x16x16_bf16 v[210:213], v[82:83], v[204:205], v[210:213]
	v_mfma_f32_16x16x16_bf16 v[210:213], v[86:87], v[84:85], v[210:213]
	v_mfma_f32_16x16x16_bf16 v[214:217], v[26:27], v[198:199], 0
	s_waitcnt lgkmcnt(13)
	v_mfma_f32_16x16x16_bf16 v[218:221], v[30:31], v[202:203], 0
	v_mfma_f32_16x16x16_bf16 v[214:217], v[28:29], v[200:201], v[214:217]
	v_mfma_f32_16x16x16_bf16 v[218:221], v[32:33], v[204:205], v[218:221]
	s_nop 2
	v_pk_add_f32 v[206:207], v[206:207], v[210:211]
	v_pk_add_f32 v[208:209], v[208:209], v[212:213]
	v_cvt_pk_bf16_f32 v242, v206, v207
	v_cvt_pk_bf16_f32 v243, v208, v209
	s_nop 1
	v_mfma_f32_16x16x16_bf16 v[238:241], v[92:93], v[242:243], 0
	v_mfma_f32_16x16x16_bf16 v[214:217], v[88:89], v[84:85], v[214:217]
	s_waitcnt lgkmcnt(11)
	v_mfma_f32_16x16x16_bf16 v[2:5], v[34:35], v[84:85], v[2:5]
	v_mfma_f32_16x16x16_bf16 v[6:9], v[36:37], v[84:85], v[6:9]
	s_waitcnt lgkmcnt(9)
	v_mfma_f32_16x16x16_bf16 v[10:13], v[38:39], v[84:85], v[10:13]
	v_mfma_f32_16x16x16_bf16 v[14:17], v[40:41], v[84:85], v[14:17]
	s_nop 0
	v_cvt_pk_bf16_f32 v244, -v238, -v239
	v_cvt_pk_bf16_f32 v245, -v240, -v241
	s_waitcnt lgkmcnt(7)
	s_nop 0
	v_mfma_f32_16x16x16_bf16 v[2:5], v[42:43], v[244:245], v[2:5]
	v_mfma_f32_16x16x16_bf16 v[6:9], v[44:45], v[244:245], v[6:9]
	s_waitcnt lgkmcnt(5)
	v_mfma_f32_16x16x16_bf16 v[10:13], v[46:47], v[244:245], v[10:13]
	v_mfma_f32_16x16x16_bf16 v[14:17], v[48:49], v[244:245], v[14:17]
	v_mfma_f32_16x16x16_bf16 v[218:221], v[90:91], v[244:245], v[218:221]
	s_nop 2
	v_mul_f32_dpp v2, v51, v2 row_newbcast:0 row_mask:0xf bank_mask:0xf
	v_mul_f32_dpp v3, v51, v3 row_newbcast:1 row_mask:0xf bank_mask:0xf
	v_mul_f32_dpp v4, v51, v4 row_newbcast:2 row_mask:0xf bank_mask:0xf
	v_mul_f32_dpp v5, v51, v5 row_newbcast:3 row_mask:0xf bank_mask:0xf
	v_mul_f32_dpp v6, v51, v6 row_newbcast:4 row_mask:0xf bank_mask:0xf
	v_mul_f32_dpp v7, v51, v7 row_newbcast:5 row_mask:0xf bank_mask:0xf
	v_mul_f32_dpp v8, v51, v8 row_newbcast:6 row_mask:0xf bank_mask:0xf
	v_mul_f32_dpp v9, v51, v9 row_newbcast:7 row_mask:0xf bank_mask:0xf
	v_mul_f32_dpp v10, v51, v10 row_newbcast:8 row_mask:0xf bank_mask:0xf
	v_mul_f32_dpp v11, v51, v11 row_newbcast:9 row_mask:0xf bank_mask:0xf
	v_mul_f32_dpp v12, v51, v12 row_newbcast:10 row_mask:0xf bank_mask:0xf
	v_mul_f32_dpp v13, v51, v13 row_newbcast:11 row_mask:0xf bank_mask:0xf
	v_mul_f32_dpp v14, v51, v14 row_newbcast:12 row_mask:0xf bank_mask:0xf
	v_mul_f32_dpp v15, v51, v15 row_newbcast:13 row_mask:0xf bank_mask:0xf
	v_mul_f32_dpp v16, v51, v16 row_newbcast:14 row_mask:0xf bank_mask:0xf
	v_mul_f32_dpp v17, v51, v17 row_newbcast:15 row_mask:0xf bank_mask:0xf
	v_pk_add_f32 v[214:215], v[214:215], v[218:219]
	v_pk_add_f32 v[216:217], v[216:217], v[220:221]
	ds_write2st64_b32 v253, v214, v215 offset0:16 offset1:17
	ds_write2st64_b32 v253, v216, v217 offset0:18 offset1:19
	s_branch .Lscan_join1

.LBB0_1140:
.Lscan_join1:
	s_waitcnt lgkmcnt(0)
	s_barrier
	v_readlane_b32 s0, v255, 17
	v_readlane_b32 s1, v255, 18
	s_and_b64 vcc, exec, s[0:1]
	s_mov_b64 s[76:77], -1
	s_cbranch_vccnz .LBB0_1142
	v_readlane_b32 s0, v255, 13
	s_nop 1
	s_xor_b32 s0, s0, 1
	s_mul_i32 s1, s0, 0x1e00
	s_lshl_b32 s0, s0, 13
	v_add_u32_e32 v252, s1, v166
	v_add_u32_e32 v253, s0, v165
	ds_read2_b64 v[68:71], v252 offset1:80
	v_cvt_pk_bf16_f32 v198, v2, v3
	v_cvt_pk_bf16_f32 v199, v4, v5
	v_cvt_pk_bf16_f32 v202, v10, v11
	v_cvt_pk_bf16_f32 v203, v12, v13
	v_cvt_pk_bf16_f32 v200, v6, v7
	v_cvt_pk_bf16_f32 v201, v8, v9
	v_cvt_pk_bf16_f32 v204, v14, v15
	v_cvt_pk_bf16_f32 v205, v16, v17
	ds_read2_b64 v[26:29], v247 offset1:4
	ds_read2_b64 v[30:33], v247 offset0:8 offset1:12
	ds_read2_b64 v[72:75], v252 offset0:160 offset1:240
	v_mfma_f32_16x16x16_bf16 v[206:209], v[18:19], v[198:199], 0
	v_mfma_f32_16x16x16_bf16 v[210:213], v[22:23], v[202:203], 0
	ds_read_b64_tr_b16 v[34:35], v248 offset:9216
	ds_read_b64_tr_b16 v[36:37], v248 offset:9248
	ds_read_b64_tr_b16 v[38:39], v248 offset:9280
	ds_read_b64_tr_b16 v[40:41], v248 offset:9312
	v_mfma_f32_16x16x16_bf16 v[206:209], v[20:21], v[200:201], v[206:209]
	v_mfma_f32_16x16x16_bf16 v[210:213], v[24:25], v[204:205], v[210:213]
	ds_read_b64_tr_b16 v[42:43], v248 offset:13824
	ds_read_b64_tr_b16 v[44:45], v248 offset:13856
	ds_read_b64_tr_b16 v[46:47], v248 offset:13888
	ds_read_b64_tr_b16 v[48:49], v248 offset:13920
	s_waitcnt lgkmcnt(11)
	v_mfma_f32_16x16x16_bf16 v[210:213], v[68:69], v[66:67], v[210:213]
	s_waitcnt lgkmcnt(10)
	v_mfma_f32_16x16x16_bf16 v[214:217], v[26:27], v[198:199], 0
	s_waitcnt lgkmcnt(9)
	v_mfma_f32_16x16x16_bf16 v[218:221], v[30:31], v[202:203], 0
	v_mfma_f32_16x16x16_bf16 v[214:217], v[28:29], v[200:201], v[214:217]
	v_mfma_f32_16x16x16_bf16 v[218:221], v[32:33], v[204:205], v[218:221]
	ds_read_b32 v50, v251 offset:33792
	ds_read_b32 v51, v251 offset:34048
	v_add_u32_e32 v246, 0x900, v246
	ds_read2_b64 v[76:79], v246 offset1:4
	ds_read2_b64 v[80:83], v246 offset0:8 offset1:12
	v_pk_add_f32 v[206:207], v[206:207], v[210:211]
	v_pk_add_f32 v[208:209], v[208:209], v[212:213]
	v_cvt_pk_bf16_f32 v242, v206, v207
	v_cvt_pk_bf16_f32 v243, v208, v209
	ds_read_b64_tr_b16 v[84:85], v250 offset:20736
	v_add_u32_e32 v252, 0xf00, v252
	s_waitcnt lgkmcnt(13)
	ds_read2_b64 v[86:89], v252 offset1:80
	v_mfma_f32_16x16x16_bf16 v[238:241], v[74:75], v[242:243], 0
	v_mfma_f32_16x16x16_bf16 v[214:217], v[70:71], v[66:67], v[214:217]
	s_waitcnt lgkmcnt(12)
	v_mfma_f32_16x16x16_bf16 v[2:5], v[34:35], v[66:67], v[2:5]
	v_mfma_f32_16x16x16_bf16 v[6:9], v[36:37], v[66:67], v[6:9]
	s_waitcnt lgkmcnt(10)
	v_mfma_f32_16x16x16_bf16 v[10:13], v[38:39], v[66:67], v[10:13]
	v_mfma_f32_16x16x16_bf16 v[14:17], v[40:41], v[66:67], v[14:17]
	ds_read2_b64 v[90:93], v252 offset0:160 offset1:240
	v_add_u32_e32 v247, 0x900, v247
	ds_read2_b64 v[26:29], v247 offset1:4
	ds_read2_b64 v[30:33], v247 offset0:8 offset1:12
	v_cvt_pk_bf16_f32 v244, -v238, -v239
	v_cvt_pk_bf16_f32 v245, -v240, -v241
	ds_read_b64_tr_b16 v[34:35], v248 offset:11520
	s_waitcnt lgkmcnt(13)
	ds_read_b64_tr_b16 v[36:37], v248 offset:11552
	s_waitcnt lgkmcnt(13)
	ds_read_b64_tr_b16 v[38:39], v248 offset:11584
	s_waitcnt lgkmcnt(13)
	ds_read_b64_tr_b16 v[40:41], v248 offset:11616
	v_mfma_f32_16x16x16_bf16 v[2:5], v[42:43], v[244:245], v[2:5]
	v_mfma_f32_16x16x16_bf16 v[6:9], v[44:45], v[244:245], v[6:9]
	s_waitcnt lgkmcnt(13)
	v_mfma_f32_16x16x16_bf16 v[10:13], v[46:47], v[244:245], v[10:13]
	v_mfma_f32_16x16x16_bf16 v[14:17], v[48:49], v[244:245], v[14:17]
	v_mfma_f32_16x16x16_bf16 v[218:221], v[72:73], v[244:245], v[218:221]
	ds_read_b64_tr_b16 v[42:43], v248 offset:16128
	s_waitcnt lgkmcnt(13)
	ds_read_b64_tr_b16 v[44:45], v248 offset:16160
	s_waitcnt lgkmcnt(13)
	ds_read_b64_tr_b16 v[46:47], v248 offset:16192
	s_waitcnt lgkmcnt(13)
	ds_read_b64_tr_b16 v[48:49], v248 offset:16224
	v_mul_f32_dpp v2, v50, v2 row_newbcast:0 row_mask:0xf bank_mask:0xf
	v_mul_f32_dpp v3, v50, v3 row_newbcast:1 row_mask:0xf bank_mask:0xf
	v_mul_f32_dpp v4, v50, v4 row_newbcast:2 row_mask:0xf bank_mask:0xf
	v_mul_f32_dpp v5, v50, v5 row_newbcast:3 row_mask:0xf bank_mask:0xf
	v_mul_f32_dpp v6, v50, v6 row_newbcast:4 row_mask:0xf bank_mask:0xf
	v_mul_f32_dpp v7, v50, v7 row_newbcast:5 row_mask:0xf bank_mask:0xf
	v_mul_f32_dpp v8, v50, v8 row_newbcast:6 row_mask:0xf bank_mask:0xf
	v_mul_f32_dpp v9, v50, v9 row_newbcast:7 row_mask:0xf bank_mask:0xf
	v_mul_f32_dpp v10, v50, v10 row_newbcast:8 row_mask:0xf bank_mask:0xf
	v_mul_f32_dpp v11, v50, v11 row_newbcast:9 row_mask:0xf bank_mask:0xf
	v_mul_f32_dpp v12, v50, v12 row_newbcast:10 row_mask:0xf bank_mask:0xf
	v_mul_f32_dpp v13, v50, v13 row_newbcast:11 row_mask:0xf bank_mask:0xf
	v_mul_f32_dpp v14, v50, v14 row_newbcast:12 row_mask:0xf bank_mask:0xf
	v_mul_f32_dpp v15, v50, v15 row_newbcast:13 row_mask:0xf bank_mask:0xf
	v_mul_f32_dpp v16, v50, v16 row_newbcast:14 row_mask:0xf bank_mask:0xf
	v_mul_f32_dpp v17, v50, v17 row_newbcast:15 row_mask:0xf bank_mask:0xf
	v_pk_add_f32 v[214:215], v[214:215], v[218:219]
	v_pk_add_f32 v[216:217], v[216:217], v[220:221]
	s_waitcnt lgkmcnt(13)
	ds_write2st64_b32 v253, v214, v215 offset0:0 offset1:1
	s_waitcnt lgkmcnt(13)
	ds_write2st64_b32 v253, v216, v217 offset0:2 offset1:3
	v_cvt_pk_bf16_f32 v198, v2, v3
	v_cvt_pk_bf16_f32 v199, v4, v5
	v_cvt_pk_bf16_f32 v202, v10, v11
	v_cvt_pk_bf16_f32 v203, v12, v13
	v_cvt_pk_bf16_f32 v200, v6, v7
	v_cvt_pk_bf16_f32 v201, v8, v9
	v_cvt_pk_bf16_f32 v204, v14, v15
	v_cvt_pk_bf16_f32 v205, v16, v17
	v_add_u32_e32 v246, v115, v155
	v_bfe_u32 v248, v0, 4, 2
	v_mul_u32_u24_e32 v248, 0x240, v248
	v_bfe_u32 v249, v0, 2, 2
	v_mul_u32_u24_e32 v249, 0x90, v249
	v_and_b32_e32 v250, 3, v0
	v_add_u32_e32 v248, v248, v249
	v_lshl_add_u32 v248, v250, 3, v248
	v_bfe_u32 v249, v0, 6, 2
	v_add_u32_e32 v246, 0x10c00, v246
	v_add_u32_e32 v248, 0x10c00, v248
	v_and_b32_e32 v251, 12, v0
	v_lshl_add_u32 v251, v251, 4, v113
	v_lshl_add_u32 v251, v250, 2, v251
	v_add_u32_e32 v251, 0x10c00, v251
	v_lshl_add_u32 v250, v249, 5, v248
	v_add_u32_e32 v247, 0x1200, v246
	s_waitcnt lgkmcnt(13)
	ds_read2_b64 v[18:21], v246 offset1:4
	s_waitcnt lgkmcnt(13)
	ds_read2_b64 v[22:25], v246 offset0:8 offset1:12
	s_waitcnt lgkmcnt(13)
	ds_read_b64_tr_b16 v[66:67], v250 offset:18432
	v_mfma_f32_16x16x16_bf16 v[206:209], v[76:77], v[198:199], 0
	v_mfma_f32_16x16x16_bf16 v[210:213], v[80:81], v[202:203], 0
	v_mfma_f32_16x16x16_bf16 v[206:209], v[78:79], v[200:201], v[206:209]
	v_mfma_f32_16x16x16_bf16 v[210:213], v[82:83], v[204:205], v[210:213]
	v_mfma_f32_16x16x16_bf16 v[210:213], v[86:87], v[84:85], v[210:213]
	v_mfma_f32_16x16x16_bf16 v[214:217], v[26:27], v[198:199], 0
	s_waitcnt lgkmcnt(13)
	v_mfma_f32_16x16x16_bf16 v[218:221], v[30:31], v[202:203], 0
	v_mfma_f32_16x16x16_bf16 v[214:217], v[28:29], v[200:201], v[214:217]
	v_mfma_f32_16x16x16_bf16 v[218:221], v[32:33], v[204:205], v[218:221]
	s_nop 2
	v_pk_add_f32 v[206:207], v[206:207], v[210:211]
	v_pk_add_f32 v[208:209], v[208:209], v[212:213]
	v_cvt_pk_bf16_f32 v242, v206, v207
	v_cvt_pk_bf16_f32 v243, v208, v209
	s_nop 1
	v_mfma_f32_16x16x16_bf16 v[238:241], v[92:93], v[242:243], 0
	v_mfma_f32_16x16x16_bf16 v[214:217], v[88:89], v[84:85], v[214:217]
	s_waitcnt lgkmcnt(11)
	v_mfma_f32_16x16x16_bf16 v[2:5], v[34:35], v[84:85], v[2:5]
	v_mfma_f32_16x16x16_bf16 v[6:9], v[36:37], v[84:85], v[6:9]
	s_waitcnt lgkmcnt(9)
	v_mfma_f32_16x16x16_bf16 v[10:13], v[38:39], v[84:85], v[10:13]
	v_mfma_f32_16x16x16_bf16 v[14:17], v[40:41], v[84:85], v[14:17]
	s_nop 0
	v_cvt_pk_bf16_f32 v244, -v238, -v239
	v_cvt_pk_bf16_f32 v245, -v240, -v241
	s_waitcnt lgkmcnt(7)
	s_nop 0
	v_mfma_f32_16x16x16_bf16 v[2:5], v[42:43], v[244:245], v[2:5]
	v_mfma_f32_16x16x16_bf16 v[6:9], v[44:45], v[244:245], v[6:9]
	s_waitcnt lgkmcnt(5)
	v_mfma_f32_16x16x16_bf16 v[10:13], v[46:47], v[244:245], v[10:13]
	v_mfma_f32_16x16x16_bf16 v[14:17], v[48:49], v[244:245], v[14:17]
	v_mfma_f32_16x16x16_bf16 v[218:221], v[90:91], v[244:245], v[218:221]
	s_nop 2
	v_mul_f32_dpp v2, v51, v2 row_newbcast:0 row_mask:0xf bank_mask:0xf
	v_mul_f32_dpp v3, v51, v3 row_newbcast:1 row_mask:0xf bank_mask:0xf
	v_mul_f32_dpp v4, v51, v4 row_newbcast:2 row_mask:0xf bank_mask:0xf
	v_mul_f32_dpp v5, v51, v5 row_newbcast:3 row_mask:0xf bank_mask:0xf
	v_mul_f32_dpp v6, v51, v6 row_newbcast:4 row_mask:0xf bank_mask:0xf
	v_mul_f32_dpp v7, v51, v7 row_newbcast:5 row_mask:0xf bank_mask:0xf
	v_mul_f32_dpp v8, v51, v8 row_newbcast:6 row_mask:0xf bank_mask:0xf
	v_mul_f32_dpp v9, v51, v9 row_newbcast:7 row_mask:0xf bank_mask:0xf
	v_mul_f32_dpp v10, v51, v10 row_newbcast:8 row_mask:0xf bank_mask:0xf
	v_mul_f32_dpp v11, v51, v11 row_newbcast:9 row_mask:0xf bank_mask:0xf
	v_mul_f32_dpp v12, v51, v12 row_newbcast:10 row_mask:0xf bank_mask:0xf
	v_mul_f32_dpp v13, v51, v13 row_newbcast:11 row_mask:0xf bank_mask:0xf
	v_mul_f32_dpp v14, v51, v14 row_newbcast:12 row_mask:0xf bank_mask:0xf
	v_mul_f32_dpp v15, v51, v15 row_newbcast:13 row_mask:0xf bank_mask:0xf
	v_mul_f32_dpp v16, v51, v16 row_newbcast:14 row_mask:0xf bank_mask:0xf
	v_mul_f32_dpp v17, v51, v17 row_newbcast:15 row_mask:0xf bank_mask:0xf
	v_pk_add_f32 v[214:215], v[214:215], v[218:219]
	v_pk_add_f32 v[216:217], v[216:217], v[220:221]
	ds_write2st64_b32 v253, v214, v215 offset0:16 offset1:17
	ds_write2st64_b32 v253, v216, v217 offset0:18 offset1:19
	s_branch .Lscan_join2

.LBB0_1160:
.Lscan_join2:
	s_waitcnt lgkmcnt(0)
	s_barrier
	v_readlane_b32 s0, v255, 17
	v_readlane_b32 s1, v255, 18
	s_and_b64 vcc, exec, s[0:1]
	s_mov_b64 s[30:31], -1
	s_cbranch_vccnz .LBB0_1162
	v_readlane_b32 s0, v255, 13
	s_nop 1
	s_nop 0
	s_mul_i32 s1, s0, 0x1e00
	s_lshl_b32 s0, s0, 13
	v_add_u32_e32 v252, s1, v166
	v_add_u32_e32 v253, s0, v165
	ds_read2_b64 v[68:71], v252 offset1:80
	v_cvt_pk_bf16_f32 v198, v2, v3
	v_cvt_pk_bf16_f32 v199, v4, v5
	v_cvt_pk_bf16_f32 v202, v10, v11
	v_cvt_pk_bf16_f32 v203, v12, v13
	v_cvt_pk_bf16_f32 v200, v6, v7
	v_cvt_pk_bf16_f32 v201, v8, v9
	v_cvt_pk_bf16_f32 v204, v14, v15
	v_cvt_pk_bf16_f32 v205, v16, v17
	ds_read2_b64 v[26:29], v247 offset1:4
	ds_read2_b64 v[30:33], v247 offset0:8 offset1:12
	ds_read2_b64 v[72:75], v252 offset0:160 offset1:240
	v_mfma_f32_16x16x16_bf16 v[206:209], v[18:19], v[198:199], 0
	v_mfma_f32_16x16x16_bf16 v[210:213], v[22:23], v[202:203], 0
	ds_read_b64_tr_b16 v[34:35], v248 offset:9216
	ds_read_b64_tr_b16 v[36:37], v248 offset:9248
	ds_read_b64_tr_b16 v[38:39], v248 offset:9280
	ds_read_b64_tr_b16 v[40:41], v248 offset:9312
	v_mfma_f32_16x16x16_bf16 v[206:209], v[20:21], v[200:201], v[206:209]
	v_mfma_f32_16x16x16_bf16 v[210:213], v[24:25], v[204:205], v[210:213]
	ds_read_b64_tr_b16 v[42:43], v248 offset:13824
	ds_read_b64_tr_b16 v[44:45], v248 offset:13856
	ds_read_b64_tr_b16 v[46:47], v248 offset:13888
	ds_read_b64_tr_b16 v[48:49], v248 offset:13920
	s_waitcnt lgkmcnt(11)
	v_mfma_f32_16x16x16_bf16 v[210:213], v[68:69], v[66:67], v[210:213]
	s_waitcnt lgkmcnt(10)
	v_mfma_f32_16x16x16_bf16 v[214:217], v[26:27], v[198:199], 0
	s_waitcnt lgkmcnt(9)
	v_mfma_f32_16x16x16_bf16 v[218:221], v[30:31], v[202:203], 0
	v_mfma_f32_16x16x16_bf16 v[214:217], v[28:29], v[200:201], v[214:217]
	v_mfma_f32_16x16x16_bf16 v[218:221], v[32:33], v[204:205], v[218:221]
	ds_read_b32 v50, v251 offset:33792
	ds_read_b32 v51, v251 offset:34048
	v_add_u32_e32 v246, 0x900, v246
	ds_read2_b64 v[76:79], v246 offset1:4
	ds_read2_b64 v[80:83], v246 offset0:8 offset1:12
	v_pk_add_f32 v[206:207], v[206:207], v[210:211]
	v_pk_add_f32 v[208:209], v[208:209], v[212:213]
	v_cvt_pk_bf16_f32 v242, v206, v207
	v_cvt_pk_bf16_f32 v243, v208, v209
	ds_read_b64_tr_b16 v[84:85], v250 offset:20736
	v_add_u32_e32 v252, 0xf00, v252
	s_waitcnt lgkmcnt(13)
	ds_read2_b64 v[86:89], v252 offset1:80
	v_mfma_f32_16x16x16_bf16 v[238:241], v[74:75], v[242:243], 0
	v_mfma_f32_16x16x16_bf16 v[214:217], v[70:71], v[66:67], v[214:217]
	s_waitcnt lgkmcnt(12)
	v_mfma_f32_16x16x16_bf16 v[2:5], v[34:35], v[66:67], v[2:5]
	v_mfma_f32_16x16x16_bf16 v[6:9], v[36:37], v[66:67], v[6:9]
	s_waitcnt lgkmcnt(10)
	v_mfma_f32_16x16x16_bf16 v[10:13], v[38:39], v[66:67], v[10:13]
	v_mfma_f32_16x16x16_bf16 v[14:17], v[40:41], v[66:67], v[14:17]
	ds_read2_b64 v[90:93], v252 offset0:160 offset1:240
	v_add_u32_e32 v247, 0x900, v247
	ds_read2_b64 v[26:29], v247 offset1:4
	ds_read2_b64 v[30:33], v247 offset0:8 offset1:12
	v_cvt_pk_bf16_f32 v244, -v238, -v239
	v_cvt_pk_bf16_f32 v245, -v240, -v241
	ds_read_b64_tr_b16 v[34:35], v248 offset:11520
	s_waitcnt lgkmcnt(13)
	ds_read_b64_tr_b16 v[36:37], v248 offset:11552
	s_waitcnt lgkmcnt(13)
	ds_read_b64_tr_b16 v[38:39], v248 offset:11584
	s_waitcnt lgkmcnt(13)
	ds_read_b64_tr_b16 v[40:41], v248 offset:11616
	v_mfma_f32_16x16x16_bf16 v[2:5], v[42:43], v[244:245], v[2:5]
	v_mfma_f32_16x16x16_bf16 v[6:9], v[44:45], v[244:245], v[6:9]
	s_waitcnt lgkmcnt(13)
	v_mfma_f32_16x16x16_bf16 v[10:13], v[46:47], v[244:245], v[10:13]
	v_mfma_f32_16x16x16_bf16 v[14:17], v[48:49], v[244:245], v[14:17]
	v_mfma_f32_16x16x16_bf16 v[218:221], v[72:73], v[244:245], v[218:221]
	ds_read_b64_tr_b16 v[42:43], v248 offset:16128
	s_waitcnt lgkmcnt(13)
	ds_read_b64_tr_b16 v[44:45], v248 offset:16160
	s_waitcnt lgkmcnt(13)
	ds_read_b64_tr_b16 v[46:47], v248 offset:16192
	s_waitcnt lgkmcnt(13)
	ds_read_b64_tr_b16 v[48:49], v248 offset:16224
	v_mul_f32_dpp v2, v50, v2 row_newbcast:0 row_mask:0xf bank_mask:0xf
	v_mul_f32_dpp v3, v50, v3 row_newbcast:1 row_mask:0xf bank_mask:0xf
	v_mul_f32_dpp v4, v50, v4 row_newbcast:2 row_mask:0xf bank_mask:0xf
	v_mul_f32_dpp v5, v50, v5 row_newbcast:3 row_mask:0xf bank_mask:0xf
	v_mul_f32_dpp v6, v50, v6 row_newbcast:4 row_mask:0xf bank_mask:0xf
	v_mul_f32_dpp v7, v50, v7 row_newbcast:5 row_mask:0xf bank_mask:0xf
	v_mul_f32_dpp v8, v50, v8 row_newbcast:6 row_mask:0xf bank_mask:0xf
	v_mul_f32_dpp v9, v50, v9 row_newbcast:7 row_mask:0xf bank_mask:0xf
	v_mul_f32_dpp v10, v50, v10 row_newbcast:8 row_mask:0xf bank_mask:0xf
	v_mul_f32_dpp v11, v50, v11 row_newbcast:9 row_mask:0xf bank_mask:0xf
	v_mul_f32_dpp v12, v50, v12 row_newbcast:10 row_mask:0xf bank_mask:0xf
	v_mul_f32_dpp v13, v50, v13 row_newbcast:11 row_mask:0xf bank_mask:0xf
	v_mul_f32_dpp v14, v50, v14 row_newbcast:12 row_mask:0xf bank_mask:0xf
	v_mul_f32_dpp v15, v50, v15 row_newbcast:13 row_mask:0xf bank_mask:0xf
	v_mul_f32_dpp v16, v50, v16 row_newbcast:14 row_mask:0xf bank_mask:0xf
	v_mul_f32_dpp v17, v50, v17 row_newbcast:15 row_mask:0xf bank_mask:0xf
	v_pk_add_f32 v[214:215], v[214:215], v[218:219]
	v_pk_add_f32 v[216:217], v[216:217], v[220:221]
	s_waitcnt lgkmcnt(13)
	ds_write2st64_b32 v253, v214, v215 offset0:0 offset1:1
	s_waitcnt lgkmcnt(13)
	ds_write2st64_b32 v253, v216, v217 offset0:2 offset1:3
	v_cvt_pk_bf16_f32 v198, v2, v3
	v_cvt_pk_bf16_f32 v199, v4, v5
	v_cvt_pk_bf16_f32 v202, v10, v11
	v_cvt_pk_bf16_f32 v203, v12, v13
	v_cvt_pk_bf16_f32 v200, v6, v7
	v_cvt_pk_bf16_f32 v201, v8, v9
	v_cvt_pk_bf16_f32 v204, v14, v15
	v_cvt_pk_bf16_f32 v205, v16, v17
	v_add_u32_e32 v246, v115, v155
	v_bfe_u32 v248, v0, 4, 2
	v_mul_u32_u24_e32 v248, 0x240, v248
	v_bfe_u32 v249, v0, 2, 2
	v_mul_u32_u24_e32 v249, 0x90, v249
	v_and_b32_e32 v250, 3, v0
	v_add_u32_e32 v248, v248, v249
	v_lshl_add_u32 v248, v250, 3, v248
	v_bfe_u32 v249, v0, 6, 2
	v_and_b32_e32 v251, 12, v0
	v_lshl_add_u32 v251, v251, 4, v113
	v_lshl_add_u32 v251, v250, 2, v251
	v_lshl_add_u32 v250, v249, 5, v248
	v_add_u32_e32 v247, 0x1200, v246
	s_waitcnt lgkmcnt(13)
	ds_read2_b64 v[18:21], v246 offset1:4
	s_waitcnt lgkmcnt(13)
	ds_read2_b64 v[22:25], v246 offset0:8 offset1:12
	s_waitcnt lgkmcnt(13)
	ds_read_b64_tr_b16 v[66:67], v250 offset:18432
	v_mfma_f32_16x16x16_bf16 v[206:209], v[76:77], v[198:199], 0
	v_mfma_f32_16x16x16_bf16 v[210:213], v[80:81], v[202:203], 0
	v_mfma_f32_16x16x16_bf16 v[206:209], v[78:79], v[200:201], v[206:209]
	v_mfma_f32_16x16x16_bf16 v[210:213], v[82:83], v[204:205], v[210:213]
	v_mfma_f32_16x16x16_bf16 v[210:213], v[86:87], v[84:85], v[210:213]
	v_mfma_f32_16x16x16_bf16 v[214:217], v[26:27], v[198:199], 0
	s_waitcnt lgkmcnt(13)
	v_mfma_f32_16x16x16_bf16 v[218:221], v[30:31], v[202:203], 0
	v_mfma_f32_16x16x16_bf16 v[214:217], v[28:29], v[200:201], v[214:217]
	v_mfma_f32_16x16x16_bf16 v[218:221], v[32:33], v[204:205], v[218:221]
	s_nop 2
	v_pk_add_f32 v[206:207], v[206:207], v[210:211]
	v_pk_add_f32 v[208:209], v[208:209], v[212:213]
	v_cvt_pk_bf16_f32 v242, v206, v207
	v_cvt_pk_bf16_f32 v243, v208, v209
	s_nop 1
	v_mfma_f32_16x16x16_bf16 v[238:241], v[92:93], v[242:243], 0
	v_mfma_f32_16x16x16_bf16 v[214:217], v[88:89], v[84:85], v[214:217]
	s_waitcnt lgkmcnt(11)
	v_mfma_f32_16x16x16_bf16 v[2:5], v[34:35], v[84:85], v[2:5]
	v_mfma_f32_16x16x16_bf16 v[6:9], v[36:37], v[84:85], v[6:9]
	s_waitcnt lgkmcnt(9)
	v_mfma_f32_16x16x16_bf16 v[10:13], v[38:39], v[84:85], v[10:13]
	v_mfma_f32_16x16x16_bf16 v[14:17], v[40:41], v[84:85], v[14:17]
	s_nop 0
	v_cvt_pk_bf16_f32 v244, -v238, -v239
	v_cvt_pk_bf16_f32 v245, -v240, -v241
	s_waitcnt lgkmcnt(7)
	s_nop 0
	v_mfma_f32_16x16x16_bf16 v[2:5], v[42:43], v[244:245], v[2:5]
	v_mfma_f32_16x16x16_bf16 v[6:9], v[44:45], v[244:245], v[6:9]
	s_waitcnt lgkmcnt(5)
	v_mfma_f32_16x16x16_bf16 v[10:13], v[46:47], v[244:245], v[10:13]
	v_mfma_f32_16x16x16_bf16 v[14:17], v[48:49], v[244:245], v[14:17]
	v_mfma_f32_16x16x16_bf16 v[218:221], v[90:91], v[244:245], v[218:221]
	s_nop 2
	v_mul_f32_dpp v2, v51, v2 row_newbcast:0 row_mask:0xf bank_mask:0xf
	v_mul_f32_dpp v3, v51, v3 row_newbcast:1 row_mask:0xf bank_mask:0xf
	v_mul_f32_dpp v4, v51, v4 row_newbcast:2 row_mask:0xf bank_mask:0xf
	v_mul_f32_dpp v5, v51, v5 row_newbcast:3 row_mask:0xf bank_mask:0xf
	v_mul_f32_dpp v6, v51, v6 row_newbcast:4 row_mask:0xf bank_mask:0xf
	v_mul_f32_dpp v7, v51, v7 row_newbcast:5 row_mask:0xf bank_mask:0xf
	v_mul_f32_dpp v8, v51, v8 row_newbcast:6 row_mask:0xf bank_mask:0xf
	v_mul_f32_dpp v9, v51, v9 row_newbcast:7 row_mask:0xf bank_mask:0xf
	v_mul_f32_dpp v10, v51, v10 row_newbcast:8 row_mask:0xf bank_mask:0xf
	v_mul_f32_dpp v11, v51, v11 row_newbcast:9 row_mask:0xf bank_mask:0xf
	v_mul_f32_dpp v12, v51, v12 row_newbcast:10 row_mask:0xf bank_mask:0xf
	v_mul_f32_dpp v13, v51, v13 row_newbcast:11 row_mask:0xf bank_mask:0xf
	v_mul_f32_dpp v14, v51, v14 row_newbcast:12 row_mask:0xf bank_mask:0xf
	v_mul_f32_dpp v15, v51, v15 row_newbcast:13 row_mask:0xf bank_mask:0xf
	v_mul_f32_dpp v16, v51, v16 row_newbcast:14 row_mask:0xf bank_mask:0xf
	v_mul_f32_dpp v17, v51, v17 row_newbcast:15 row_mask:0xf bank_mask:0xf
	v_pk_add_f32 v[214:215], v[214:215], v[218:219]
	v_pk_add_f32 v[216:217], v[216:217], v[220:221]
	ds_write2st64_b32 v253, v214, v215 offset0:16 offset1:17
	ds_write2st64_b32 v253, v216, v217 offset0:18 offset1:19
	s_branch .Lscan_join3
